# baseline (speedup 1.0000x reference)
_Z5k_aggILb0ELi4ELb1EEvPK15HIP_vector_typeIjLj4EEPKS0_IiLj2EEPKiS8_PKfSA_PKDv8_DF16_PDF16_Pf:
	s_cmpk_gt_u32 s2, 0x7ff
	s_cbranch_scc1 .Lpw2_exit
	s_mov_b32 s70, s0
	s_mov_b32 s71, s1
	s_mov_b32 s72, s2
	v_readfirstlane_b32 s73, v0
	s_lshr_b32 s73, s73, 6

.LBB2_101:
.Lpw2_tail:
	s_mov_b64 exec, -1
	s_addk_i32 s72, 0x800
	s_cmpk_lt_u32 s72, 0xc35
	s_cbranch_scc0 .Lpw2_exit
	s_waitcnt lgkmcnt(0)
	s_barrier
	s_mov_b32 s0, s70
	s_mov_b32 s1, s71
	s_mov_b32 s2, s72
	v_mbcnt_lo_u32_b32 v0, -1, 0
	v_mbcnt_hi_u32_b32 v0, -1, v0
	v_lshl_or_b32 v0, s73, 6, v0
	s_branch .Lpw2_top

	.amdhsa_kernel _Z5k_aggILb0ELi4ELb1EEvPK15HIP_vector_typeIjLj4EEPKS0_IiLj2EEPKiS8_PKfSA_PKDv8_DF16_PDF16_Pf
		.amdhsa_group_segment_fixed_size 17472
		.amdhsa_private_segment_fixed_size 0
		.amdhsa_kernarg_size 72
		.amdhsa_user_sgpr_count 2
		.amdhsa_user_sgpr_dispatch_ptr 0
		.amdhsa_user_sgpr_queue_ptr 0
		.amdhsa_user_sgpr_kernarg_segment_ptr 1
		.amdhsa_user_sgpr_dispatch_id 0
		.amdhsa_user_sgpr_kernarg_preload_length 0
		.amdhsa_user_sgpr_kernarg_preload_offset 0
		.amdhsa_user_sgpr_private_segment_size 0
		.amdhsa_uses_dynamic_stack 0
		.amdhsa_enable_private_segment 0
		.amdhsa_system_sgpr_workgroup_id_x 1
		.amdhsa_system_sgpr_workgroup_id_y 0
		.amdhsa_system_sgpr_workgroup_id_z 0
		.amdhsa_system_sgpr_workgroup_info 0
		.amdhsa_system_vgpr_workitem_id 0
		.amdhsa_next_free_vgpr 64
		.amdhsa_next_free_sgpr 74
		.amdhsa_accum_offset 64
		.amdhsa_reserve_vcc 1
		.amdhsa_float_round_mode_32 0
		.amdhsa_float_round_mode_16_64 0
		.amdhsa_float_denorm_mode_32 3
		.amdhsa_float_denorm_mode_16_64 3
		.amdhsa_dx10_clamp 1
		.amdhsa_ieee_mode 1
		.amdhsa_fp16_overflow 0
		.amdhsa_tg_split 0
		.amdhsa_exception_fp_ieee_invalid_op 0
		.amdhsa_exception_fp_denorm_src 0
		.amdhsa_exception_fp_ieee_div_zero 0
		.amdhsa_exception_fp_ieee_overflow 0
		.amdhsa_exception_fp_ieee_underflow 0
		.amdhsa_exception_fp_ieee_inexact 0
		.amdhsa_exception_int_div_zero 0
	.end_amdhsa_kernel

_Z5k_aggILb0ELi4ELb0EEvPK15HIP_vector_typeIjLj4EEPKS0_IiLj2EEPKiS8_PKfSA_PKDv8_DF16_PDF16_Pf:
	s_cmpk_gt_u32 s2, 0x7ff
	s_cbranch_scc1 .Lpw3_exit
	s_mov_b32 s70, s0
	s_mov_b32 s71, s1
	s_mov_b32 s72, s2
	v_readfirstlane_b32 s73, v0
	s_lshr_b32 s73, s73, 6

	.amdhsa_kernel _Z5k_aggILb0ELi4ELb0EEvPK15HIP_vector_typeIjLj4EEPKS0_IiLj2EEPKiS8_PKfSA_PKDv8_DF16_PDF16_Pf
		.amdhsa_group_segment_fixed_size 17472
		.amdhsa_private_segment_fixed_size 0
		.amdhsa_kernarg_size 72
		.amdhsa_user_sgpr_count 2
		.amdhsa_user_sgpr_dispatch_ptr 0
		.amdhsa_user_sgpr_queue_ptr 0
		.amdhsa_user_sgpr_kernarg_segment_ptr 1
		.amdhsa_user_sgpr_dispatch_id 0
		.amdhsa_user_sgpr_kernarg_preload_length 0
		.amdhsa_user_sgpr_kernarg_preload_offset 0
		.amdhsa_user_sgpr_private_segment_size 0
		.amdhsa_uses_dynamic_stack 0
		.amdhsa_enable_private_segment 0
		.amdhsa_system_sgpr_workgroup_id_x 1
		.amdhsa_system_sgpr_workgroup_id_y 0
		.amdhsa_system_sgpr_workgroup_id_z 0
		.amdhsa_system_sgpr_workgroup_info 0
		.amdhsa_system_vgpr_workitem_id 0
		.amdhsa_next_free_vgpr 62
		.amdhsa_next_free_sgpr 74
		.amdhsa_accum_offset 64
		.amdhsa_reserve_vcc 1
		.amdhsa_float_round_mode_32 0
		.amdhsa_float_round_mode_16_64 0
		.amdhsa_float_denorm_mode_32 3
		.amdhsa_float_denorm_mode_16_64 3
		.amdhsa_dx10_clamp 1
		.amdhsa_ieee_mode 1
		.amdhsa_fp16_overflow 0
		.amdhsa_tg_split 0
		.amdhsa_exception_fp_ieee_invalid_op 0
		.amdhsa_exception_fp_denorm_src 0
		.amdhsa_exception_fp_ieee_div_zero 0
		.amdhsa_exception_fp_ieee_overflow 0
		.amdhsa_exception_fp_ieee_underflow 0
		.amdhsa_exception_fp_ieee_inexact 0
		.amdhsa_exception_int_div_zero 0
	.end_amdhsa_kernel

_Z5k_aggILb1ELi4ELb0EEvPK15HIP_vector_typeIjLj4EEPKS0_IiLj2EEPKiS8_PKfSA_PKDv8_DF16_PDF16_Pf:
	s_cmpk_gt_u32 s2, 0x7ff
	s_cbranch_scc1 .Lpw4_exit
	s_mov_b32 s70, s0
	s_mov_b32 s71, s1
	s_mov_b32 s72, s2
	v_readfirstlane_b32 s73, v0
	s_lshr_b32 s73, s73, 6

.LBB4_97:
	s_branch .Lpw4_tail

.Lpw4_tail:
	s_mov_b64 exec, -1
	s_addk_i32 s72, 0x800
	s_cmpk_lt_u32 s72, 0xc35
	s_cbranch_scc0 .Lpw4_exit
	s_waitcnt lgkmcnt(0)
	s_barrier
	s_mov_b32 s0, s70
	s_mov_b32 s1, s71
	s_mov_b32 s2, s72
	v_mbcnt_lo_u32_b32 v0, -1, 0
	v_mbcnt_hi_u32_b32 v0, -1, v0
	v_lshl_or_b32 v0, s73, 6, v0
	s_branch .Lpw4_top

	.amdhsa_kernel _Z5k_aggILb1ELi4ELb0EEvPK15HIP_vector_typeIjLj4EEPKS0_IiLj2EEPKiS8_PKfSA_PKDv8_DF16_PDF16_Pf
		.amdhsa_group_segment_fixed_size 17472
		.amdhsa_private_segment_fixed_size 0
		.amdhsa_kernarg_size 72
		.amdhsa_user_sgpr_count 2
		.amdhsa_user_sgpr_dispatch_ptr 0
		.amdhsa_user_sgpr_queue_ptr 0
		.amdhsa_user_sgpr_kernarg_segment_ptr 1
		.amdhsa_user_sgpr_dispatch_id 0
		.amdhsa_user_sgpr_kernarg_preload_length 0
		.amdhsa_user_sgpr_kernarg_preload_offset 0
		.amdhsa_user_sgpr_private_segment_size 0
		.amdhsa_uses_dynamic_stack 0
		.amdhsa_enable_private_segment 0
		.amdhsa_system_sgpr_workgroup_id_x 1
		.amdhsa_system_sgpr_workgroup_id_y 0
		.amdhsa_system_sgpr_workgroup_id_z 0
		.amdhsa_system_sgpr_workgroup_info 0
		.amdhsa_system_vgpr_workitem_id 0
		.amdhsa_next_free_vgpr 62
		.amdhsa_next_free_sgpr 74
		.amdhsa_accum_offset 64
		.amdhsa_reserve_vcc 1
		.amdhsa_float_round_mode_32 0
		.amdhsa_float_round_mode_16_64 0
		.amdhsa_float_denorm_mode_32 3
		.amdhsa_float_denorm_mode_16_64 3
		.amdhsa_dx10_clamp 1
		.amdhsa_ieee_mode 1
		.amdhsa_fp16_overflow 0
		.amdhsa_tg_split 0
		.amdhsa_exception_fp_ieee_invalid_op 0
		.amdhsa_exception_fp_denorm_src 0
		.amdhsa_exception_fp_ieee_div_zero 0
		.amdhsa_exception_fp_ieee_overflow 0
		.amdhsa_exception_fp_ieee_underflow 0
		.amdhsa_exception_fp_ieee_inexact 0
		.amdhsa_exception_int_div_zero 0
	.end_amdhsa_kernel

amdhsa.kernels:
  - .agpr_count:     0
    .args:
      - .actual_access:  read_only
        .address_space:  global
        .offset:         0
        .size:           8
        .value_kind:     global_buffer
      - .actual_access:  read_only
        .address_space:  global
        .offset:         8
        .size:           8
        .value_kind:     global_buffer
      - .actual_access:  read_only
        .address_space:  global
        .offset:         16
        .size:           8
        .value_kind:     global_buffer
      - .actual_access:  read_only
        .address_space:  global
        .offset:         24
        .size:           8
        .value_kind:     global_buffer
      - .actual_access:  read_only
        .address_space:  global
        .offset:         32
        .size:           8
        .value_kind:     global_buffer
      - .actual_access:  write_only
        .address_space:  global
        .offset:         40
        .size:           8
        .value_kind:     global_buffer
      - .actual_access:  write_only
        .address_space:  global
        .offset:         48
        .size:           8
        .value_kind:     global_buffer
      - .actual_access:  write_only
        .address_space:  global
        .offset:         56
        .size:           8
        .value_kind:     global_buffer
      - .actual_access:  write_only
        .address_space:  global
        .offset:         64
        .size:           8
        .value_kind:     global_buffer
    .group_segment_fixed_size: 35168
    .kernarg_segment_align: 8
    .kernarg_segment_size: 72
    .language:       OpenCL C
    .language_version:
      - 2
      - 0
    .max_flat_workgroup_size: 512
    .name:           _Z6k_prepPKiPKfS2_S2_S2_PjP15HIP_vector_typeIiLj2EEPDv8_DF16_Pi
    .private_segment_fixed_size: 0
    .sgpr_count:     46
    .sgpr_spill_count: 0
    .symbol:         _Z6k_prepPKiPKfS2_S2_S2_PjP15HIP_vector_typeIiLj2EEPDv8_DF16_Pi.kd
    .uniform_work_group_size: 1
    .uses_dynamic_stack: false
    .vgpr_count:     58
    .vgpr_spill_count: 0
    .wavefront_size: 64
  - .agpr_count:     32
    .args:
      - .actual_access:  read_only
        .address_space:  global
        .offset:         0
        .size:           8
        .value_kind:     global_buffer
      - .actual_access:  read_only
        .address_space:  global
        .offset:         8
        .size:           8
        .value_kind:     global_buffer
      - .actual_access:  write_only
        .address_space:  global
        .offset:         16
        .size:           8
        .value_kind:     global_buffer
      - .actual_access:  write_only
        .address_space:  global
        .offset:         24
        .size:           8
        .value_kind:     global_buffer
      - .actual_access:  write_only
        .address_space:  global
        .offset:         32
        .size:           8
        .value_kind:     global_buffer
      - .actual_access:  write_only
        .address_space:  global
        .offset:         40
        .size:           8
        .value_kind:     global_buffer
      - .address_space:  global
        .offset:         48
        .size:           8
        .value_kind:     global_buffer
      - .actual_access:  read_only
        .address_space:  global
        .offset:         56
        .size:           8
        .value_kind:     global_buffer
      - .actual_access:  read_only
        .address_space:  global
        .offset:         64
        .size:           8
        .value_kind:     global_buffer
      - .address_space:  global
        .offset:         72
        .size:           8
        .value_kind:     global_buffer
    .group_segment_fixed_size: 38736
    .kernarg_segment_align: 8
    .kernarg_segment_size: 80
    .language:       OpenCL C
    .language_version:
      - 2
      - 0
    .max_flat_workgroup_size: 256
    .name:           _Z11k_csr_gemm1PKjPK15HIP_vector_typeIiLj2EEPS2_PiS6_PfS6_PKfPKDv8_DF16_PDF16_
    .private_segment_fixed_size: 0
    .sgpr_count:     70
    .sgpr_spill_count: 0
    .symbol:         _Z11k_csr_gemm1PKjPK15HIP_vector_typeIiLj2EEPS2_PiS6_PfS6_PKfPKDv8_DF16_PDF16_.kd
    .uniform_work_group_size: 1
    .uses_dynamic_stack: false
    .vgpr_count:     128
    .vgpr_spill_count: 0
    .wavefront_size: 64
  - .agpr_count:     0
    .args:
      - .actual_access:  read_only
        .address_space:  global
        .offset:         0
        .size:           8
        .value_kind:     global_buffer
      - .actual_access:  read_only
        .address_space:  global
        .offset:         8
        .size:           8
        .value_kind:     global_buffer
      - .actual_access:  read_only
        .address_space:  global
        .offset:         16
        .size:           8
        .value_kind:     global_buffer
      - .actual_access:  read_only
        .address_space:  global
        .offset:         24
        .size:           8
        .value_kind:     global_buffer
      - .actual_access:  read_only
        .address_space:  global
        .offset:         32
        .size:           8
        .value_kind:     global_buffer
      - .actual_access:  read_only
        .address_space:  global
        .offset:         40
        .size:           8
        .value_kind:     global_buffer
      - .actual_access:  read_only
        .address_space:  global
        .offset:         48
        .size:           8
        .value_kind:     global_buffer
      - .address_space:  global
        .offset:         56
        .size:           8
        .value_kind:     global_buffer
      - .actual_access:  read_only
        .address_space:  global
        .offset:         64
        .size:           8
        .value_kind:     global_buffer
    .group_segment_fixed_size: 17472
    .kernarg_segment_align: 8
    .kernarg_segment_size: 72
    .language:       OpenCL C
    .language_version:
      - 2
      - 0
    .max_flat_workgroup_size: 256
    .name:           _Z5k_aggILb0ELi4ELb1EEvPK15HIP_vector_typeIjLj4EEPKS0_IiLj2EEPKiS8_PKfSA_PKDv8_DF16_PDF16_Pf
    .private_segment_fixed_size: 0
    .sgpr_count:     80
    .sgpr_spill_count: 0
    .symbol:         _Z5k_aggILb0ELi4ELb1EEvPK15HIP_vector_typeIjLj4EEPKS0_IiLj2EEPKiS8_PKfSA_PKDv8_DF16_PDF16_Pf.kd
    .uniform_work_group_size: 1
    .uses_dynamic_stack: false
    .vgpr_count:     64
    .vgpr_spill_count: 0
    .wavefront_size: 64
  - .agpr_count:     0
    .args:
      - .actual_access:  read_only
        .address_space:  global
        .offset:         0
        .size:           8
        .value_kind:     global_buffer
      - .actual_access:  read_only
        .address_space:  global
        .offset:         8
        .size:           8
        .value_kind:     global_buffer
      - .actual_access:  read_only
        .address_space:  global
        .offset:         16
        .size:           8
        .value_kind:     global_buffer
      - .actual_access:  read_only
        .address_space:  global
        .offset:         24
        .size:           8
        .value_kind:     global_buffer
      - .actual_access:  read_only
        .address_space:  global
        .offset:         32
        .size:           8
        .value_kind:     global_buffer
      - .actual_access:  read_only
        .address_space:  global
        .offset:         40
        .size:           8
        .value_kind:     global_buffer
      - .actual_access:  read_only
        .address_space:  global
        .offset:         48
        .size:           8
        .value_kind:     global_buffer
      - .address_space:  global
        .offset:         56
        .size:           8
        .value_kind:     global_buffer
      - .actual_access:  read_only
        .address_space:  global
        .offset:         64
        .size:           8
        .value_kind:     global_buffer
    .group_segment_fixed_size: 17472
    .kernarg_segment_align: 8
    .kernarg_segment_size: 72
    .language:       OpenCL C
    .language_version:
      - 2
      - 0
    .max_flat_workgroup_size: 256
    .name:           _Z5k_aggILb0ELi4ELb0EEvPK15HIP_vector_typeIjLj4EEPKS0_IiLj2EEPKiS8_PKfSA_PKDv8_DF16_PDF16_Pf
    .private_segment_fixed_size: 0
    .sgpr_count:     80
    .sgpr_spill_count: 0
    .symbol:         _Z5k_aggILb0ELi4ELb0EEvPK15HIP_vector_typeIjLj4EEPKS0_IiLj2EEPKiS8_PKfSA_PKDv8_DF16_PDF16_Pf.kd
    .uniform_work_group_size: 1
    .uses_dynamic_stack: false
    .vgpr_count:     62
    .vgpr_spill_count: 0
    .wavefront_size: 64
  - .agpr_count:     0
    .args:
      - .actual_access:  read_only
        .address_space:  global
        .offset:         0
        .size:           8
        .value_kind:     global_buffer
      - .actual_access:  read_only
        .address_space:  global
        .offset:         8
        .size:           8
        .value_kind:     global_buffer
      - .actual_access:  read_only
        .address_space:  global
        .offset:         16
        .size:           8
        .value_kind:     global_buffer
      - .actual_access:  read_only
        .address_space:  global
        .offset:         24
        .size:           8
        .value_kind:     global_buffer
      - .actual_access:  read_only
        .address_space:  global
        .offset:         32
        .size:           8
        .value_kind:     global_buffer
      - .actual_access:  read_only
        .address_space:  global
        .offset:         40
        .size:           8
        .value_kind:     global_buffer
      - .actual_access:  read_only
        .address_space:  global
        .offset:         48
        .size:           8
        .value_kind:     global_buffer
      - .actual_access:  read_only
        .address_space:  global
        .offset:         56
        .size:           8
        .value_kind:     global_buffer
      - .actual_access:  write_only
        .address_space:  global
        .offset:         64
        .size:           8
        .value_kind:     global_buffer
    .group_segment_fixed_size: 17472
    .kernarg_segment_align: 8
    .kernarg_segment_size: 72
    .language:       OpenCL C
    .language_version:
      - 2
      - 0
    .max_flat_workgroup_size: 256
    .name:           _Z5k_aggILb1ELi4ELb0EEvPK15HIP_vector_typeIjLj4EEPKS0_IiLj2EEPKiS8_PKfSA_PKDv8_DF16_PDF16_Pf
    .private_segment_fixed_size: 0
    .sgpr_count:     80
    .sgpr_spill_count: 0
    .symbol:         _Z5k_aggILb1ELi4ELb0EEvPK15HIP_vector_typeIjLj4EEPKS0_IiLj2EEPKiS8_PKfSA_PKDv8_DF16_PDF16_Pf.kd
    .uniform_work_group_size: 1
    .uses_dynamic_stack: false
    .vgpr_count:     62
    .vgpr_spill_count: 0
    .wavefront_size: 64
